# v14
# speedup vs baseline: 1.0311x; 1.0021x over previous
.LBB0_15:
	s_or_b64 exec, exec, s[22:23]
	s_waitcnt vmcnt(0)
	v_max3_f32 v19, |v14|, 0, |v15|
	v_max3_f32 v19, v19, |v16|, |v17|
	v_max3_f32 v19, v19, |v10|, |v11|
	v_max3_f32 v19, v19, |v12|, |v13|
	s_nop 1
	v_max_f32_dpp v19, v19, v19 quad_perm:[1,0,3,2] row_mask:0xf bank_mask:0xf bound_ctrl:1
	s_nop 1
	v_max_f32_dpp v19, v19, v19 quad_perm:[2,3,0,1] row_mask:0xf bank_mask:0xf bound_ctrl:1
	s_nop 1
	v_max_f32_dpp v19, v19, v19 row_half_mirror row_mask:0xf bank_mask:0xf bound_ctrl:1
	s_nop 1
	v_max_f32_dpp v19, v19, v19 row_mirror row_mask:0xf bank_mask:0xf bound_ctrl:1
	v_div_scale_f32 v23, s[22:23], v19, v19, s26
	v_rcp_f32_e32 v28, v23
	v_div_scale_f32 v29, vcc, s26, v19, s26
	v_fma_f32 v30, -v23, v28, 1.0
	v_fmac_f32_e32 v28, v30, v28
	v_mul_f32_e32 v30, v29, v28
	v_fma_f32 v31, -v23, v30, v29
	v_fmac_f32_e32 v30, v31, v28
	v_fma_f32 v23, -v23, v30, v29
	v_div_fmas_f32 v23, v23, v28, v30
	v_div_fixup_f32 v23, v23, v19, s26
	v_cmp_lt_f32_e32 vcc, 0, v19
	s_nop 1
	v_cndmask_b32_e32 v23, 0, v23, vcc
	v_mul_f32_e32 v14, v14, v23
	v_mul_f32_e32 v10, v10, v23
	v_mul_f32_e32 v15, v15, v23
	v_mul_f32_e32 v11, v11, v23
	v_rndne_f32_e32 v14, v14
	v_rndne_f32_e32 v10, v10
	v_rndne_f32_e32 v15, v15
	v_rndne_f32_e32 v11, v11
	v_cvt_i32_f32_e32 v14, v14
	v_cvt_i32_f32_e32 v10, v10
	v_cvt_i32_f32_e32 v15, v15
	v_cvt_i32_f32_e32 v11, v11
	v_max_i32_e32 v14, 0xffffff81, v14
	v_max_i32_e32 v10, 0xffffff81, v10
	v_max_i32_e32 v15, 0xffffff81, v15
	v_max_i32_e32 v11, 0xffffff81, v11
	v_add_u32_e32 v14, 0x80, v14
	v_add_u32_e32 v10, 0x80, v10
	v_add_u32_e32 v15, 0x80, v15
	v_add_u32_e32 v11, 0x80, v11
	v_min_u32_e32 v14, 0xff, v14
	v_min_u32_e32 v10, 0xff, v10
	v_min_u32_e32 v15, 0xff, v15
	v_min_u32_e32 v11, 0xff, v11
	v_lshl_or_b32 v14, v15, 8, v14
	v_lshl_or_b32 v11, v11, 8, v10
	v_mul_f32_e32 v10, v16, v23
	v_mul_f32_e32 v12, v12, v23
	v_mul_f32_e32 v15, v17, v23
	v_mul_f32_e32 v13, v13, v23
	v_rndne_f32_e32 v10, v10
	v_rndne_f32_e32 v12, v12
	v_rndne_f32_e32 v15, v15
	v_rndne_f32_e32 v13, v13
	v_cvt_i32_f32_e32 v10, v10
	v_cvt_i32_f32_e32 v12, v12
	v_cvt_i32_f32_e32 v15, v15
	v_cvt_i32_f32_e32 v13, v13
	v_max_i32_e32 v10, 0xffffff81, v10
	v_max_i32_e32 v12, 0xffffff81, v12
	v_max_i32_e32 v15, 0xffffff81, v15
	v_max_i32_e32 v13, 0xffffff81, v13
	v_add_u32_e32 v10, 0x80, v10
	v_add_u32_e32 v12, 0x80, v12
	v_add_u32_e32 v15, 0x80, v15
	v_add_u32_e32 v13, 0x80, v13
	v_min_u32_sdwa v10, v10, s27 dst_sel:WORD_1 dst_unused:UNUSED_PAD src0_sel:DWORD src1_sel:DWORD
	v_min_u32_sdwa v12, v12, s27 dst_sel:WORD_1 dst_unused:UNUSED_PAD src0_sel:DWORD src1_sel:DWORD
	v_min_u32_sdwa v15, v15, s27 dst_sel:BYTE_3 dst_unused:UNUSED_PAD src0_sel:DWORD src1_sel:DWORD
	v_min_u32_sdwa v13, v13, s27 dst_sel:BYTE_3 dst_unused:UNUSED_PAD src0_sel:DWORD src1_sel:DWORD
	v_or3_b32 v10, v14, v10, v15
	v_or3_b32 v11, v11, v12, v13
	global_store_dwordx2 v[20:21], v[10:11], off offset:-4
	s_and_saveexec_b64 s[22:23], s[6:7]
	s_cbranch_execz .LBB0_17
	v_ashrrev_i32_e32 v10, 4, v18
	v_ashrrev_i32_e32 v11, 31, v10
	v_mul_f32_e32 v12, 0x41010204, v19
	v_lshl_add_u64 v[10:11], v[10:11], 2, s[12:13]
	global_store_dword v[10:11], v12, off
.LBB0_17:
	s_or_b64 exec, exec, s[22:23]
	s_and_saveexec_b64 s[22:23], s[4:5]
	s_cbranch_execz .LBB0_12
	v_max3_f32 v10, |v2|, 0, |v3|
	v_max3_f32 v10, v10, |v4|, |v5|
	v_max3_f32 v10, v10, |v6|, |v7|
	v_max3_f32 v10, v10, |v8|, |v9|
	v_ashrrev_i32_e32 v23, 31, v22
	s_nop 1
	v_max_f32_dpp v10, v10, v10 quad_perm:[1,0,3,2] row_mask:0xf bank_mask:0xf bound_ctrl:1
	s_nop 1
	v_max_f32_dpp v10, v10, v10 quad_perm:[2,3,0,1] row_mask:0xf bank_mask:0xf bound_ctrl:1
	s_nop 1
	v_max_f32_dpp v10, v10, v10 row_half_mirror row_mask:0xf bank_mask:0xf bound_ctrl:1
	s_nop 1
	v_max_f32_dpp v10, v10, v10 row_mirror row_mask:0xf bank_mask:0xf bound_ctrl:1
	v_div_scale_f32 v11, s[4:5], v10, v10, s26
	v_rcp_f32_e32 v12, v11
	v_div_scale_f32 v13, vcc, s26, v10, s26
	v_fma_f32 v14, -v11, v12, 1.0
	v_fmac_f32_e32 v12, v14, v12
	v_mul_f32_e32 v14, v13, v12
	v_fma_f32 v15, -v11, v14, v13
	v_fmac_f32_e32 v14, v15, v12
	v_fma_f32 v11, -v11, v14, v13
	v_div_fmas_f32 v11, v11, v12, v14
	v_div_fixup_f32 v11, v11, v10, s26
	v_cmp_lt_f32_e32 vcc, 0, v10
	s_nop 1
	v_cndmask_b32_e32 v11, 0, v11, vcc
	v_mul_f32_e32 v2, v2, v11
	v_mul_f32_e32 v6, v6, v11
	v_mul_f32_e32 v3, v3, v11
	v_mul_f32_e32 v7, v7, v11
	v_rndne_f32_e32 v2, v2
	v_rndne_f32_e32 v6, v6
	v_rndne_f32_e32 v3, v3
	v_rndne_f32_e32 v7, v7
	v_cvt_i32_f32_e32 v2, v2
	v_cvt_i32_f32_e32 v6, v6
	v_cvt_i32_f32_e32 v3, v3
	v_cvt_i32_f32_e32 v7, v7
	v_max_i32_e32 v2, 0xffffff81, v2
	v_max_i32_e32 v6, 0xffffff81, v6
	v_max_i32_e32 v3, 0xffffff81, v3
	v_max_i32_e32 v7, 0xffffff81, v7
	v_add_u32_e32 v2, 0x80, v2
	v_add_u32_e32 v6, 0x80, v6
	v_add_u32_e32 v3, 0x80, v3
	v_add_u32_e32 v7, 0x80, v7
	v_min_u32_e32 v2, 0xff, v2
	v_min_u32_e32 v6, 0xff, v6
	v_min_u32_e32 v3, 0xff, v3
	v_min_u32_e32 v7, 0xff, v7
	v_lshl_or_b32 v2, v3, 8, v2
	v_lshl_or_b32 v3, v7, 8, v6
	v_mul_f32_e32 v4, v4, v11
	v_mul_f32_e32 v6, v8, v11
	v_mul_f32_e32 v5, v5, v11
	v_mul_f32_e32 v7, v9, v11
	v_rndne_f32_e32 v4, v4
	v_rndne_f32_e32 v6, v6
	v_rndne_f32_e32 v5, v5
	v_rndne_f32_e32 v7, v7
	v_cvt_i32_f32_e32 v4, v4
	v_cvt_i32_f32_e32 v6, v6
	v_cvt_i32_f32_e32 v5, v5
	v_cvt_i32_f32_e32 v7, v7
	v_max_i32_e32 v4, 0xffffff81, v4
	v_max_i32_e32 v6, 0xffffff81, v6
	v_max_i32_e32 v5, 0xffffff81, v5
	v_max_i32_e32 v7, 0xffffff81, v7
	v_add_u32_e32 v4, 0x80, v4
	v_add_u32_e32 v6, 0x80, v6
	v_add_u32_e32 v5, 0x80, v5
	v_add_u32_e32 v7, 0x80, v7
	v_min_u32_sdwa v4, v4, s27 dst_sel:WORD_1 dst_unused:UNUSED_PAD src0_sel:DWORD src1_sel:DWORD
	v_min_u32_sdwa v6, v6, s27 dst_sel:WORD_1 dst_unused:UNUSED_PAD src0_sel:DWORD src1_sel:DWORD
	v_min_u32_sdwa v5, v5, s27 dst_sel:BYTE_3 dst_unused:UNUSED_PAD src0_sel:DWORD src1_sel:DWORD
	v_min_u32_sdwa v7, v7, s27 dst_sel:BYTE_3 dst_unused:UNUSED_PAD src0_sel:DWORD src1_sel:DWORD
	v_or3_b32 v2, v2, v4, v5
	v_or3_b32 v3, v3, v6, v7
	v_lshl_add_u64 v[4:5], v[22:23], 3, s[8:9]
	global_store_dwordx2 v[4:5], v[2:3], off
	s_and_b64 exec, exec, s[6:7]
	s_cbranch_execz .LBB0_12
	v_ashrrev_i32_e32 v2, 4, v22
	v_ashrrev_i32_e32 v3, 31, v2
	v_mul_f32_e32 v4, 0x41010204, v10
	v_lshl_add_u64 v[2:3], v[2:3], 2, s[12:13]
	global_store_dword v[2:3], v4, off
	s_branch .LBB0_12
